# P7 epilogue: (u+1)*SH/KP folded into the up scale, bias and clamp bounds; one packed-mul half and one subtract fewer per element
# speedup vs baseline: 1.0032x; 1.0029x over previous
; #define PG8_STAGE(bufoff, gbase, voff) do { if constexpr (!(Sched::CRIP & 2)) _Pragma("unroll") for (int _i = 0; _i < 2; ++_i) { unsigned _o = (voff)[_i]; asm volatile("" : "+v"(_o)); \
;         __builtin_amdgcn_global_load_lds((const unsigned*)((const char*)(gbase) + _o), (LAS unsigned*)(lds + (bufoff) + ldsw + _i * 8192), 16, 0, 0); } } while (0)
; #define PG8_WAIT_V(n) asm volatile("s_waitcnt vmcnt(" #n ")" ::: "memory")
; #define PG8_BAR __builtin_amdgcn_s_barrier()
; template <class Epi, class Sched>
; __device__ __forceinline__ void gemm_phase(LAS unsigned char* lds, const Sched& S, const Epi& E) {
;     ...
;     PG8_STAGE(PG8_SB(0, 0), cB + PG8_KT(crot, 0), voffB); PG8_STAGE(PG8_SB(0, 1), cB + hstep + PG8_KT(crot, 0), voffB); PG8_STAGE(PG8_SA(0, 0), cA + PG8_KT(crot, 0), vA[0]); PG8_STAGE(PG8_SA(0, 1), cA + PG8_KT(crot, 0), vA[1]);
;     if (wr == 1) PG8_BAR;
;     PG8_WAIT_V(2); PG8_BAR;
;     PG8_STAGE(PG8_SB(1, 0), cB + PG8_KT(crot, 1), voffB); PG8_STAGE(PG8_SA(1, 0), cA + PG8_KT(crot, 1), vA[0]); PG8_STAGE(PG8_SB(1, 1), cB + hstep + PG8_KT(crot, 1), voffB);
;     PG8_WAIT_V(6); PG8_BAR;
;     ...
;                 for (int i = 0; i < 2; ++i) { int R, C; stage_rc(tz * 16 + i * 8192, R, C);
; #pragma unroll
;                     for (int h = 0; h < 2; ++h) vA[h][i] = (unsigned)(lidx[h * HALF + R] * RP + C * 2); } } }
.LBB0_724:
	s_add_u32 s12, s88, 0x3a800000
	s_addc_u32 s13, s89, 0
	s_lshl_b32 s2, s2, 12
	s_addk_i32 s7, 0x80
	s_lshl_b32 s14, s3, 13
	s_and_b32 s15, s2, 0x3000
	s_and_b32 s7, s7, 0x780
	s_add_u32 s2, s28, s7
	v_mov_b32_e32 v2, v1
	s_waitcnt vmcnt(2)
	s_barrier
	s_addc_u32 s3, s29, 0
	s_add_i32 m0, s39, 0x18000
	v_lshlrev_b32_e32 v3, 6, v0
	global_load_lds_dwordx4 v2, s[2:3]
	v_mov_b32_e32 v2, v190
	s_add_i32 m0, s39, 0x1a000
	v_lshlrev_b32_e32 v5, 2, v0
	global_load_lds_dwordx4 v2, s[2:3]
	s_add_u32 s2, s58, s7
	s_addc_u32 s3, s59, 0
	v_mov_b32_e32 v2, v192
	s_add_i32 s70, s39, 0x8000
	s_mov_b32 m0, s70
	s_add_i32 s71, s39, 0xa000
	global_load_lds_dwordx4 v2, s[2:3]
	v_mov_b32_e32 v2, v194
	s_mov_b32 m0, s71
	v_and_b32_e32 v3, 0x3c0, v3
	global_load_lds_dwordx4 v2, s[2:3]
	s_add_u32 s2, s4, s7
	v_mov_b32_e32 v2, v1
	s_addc_u32 s3, s5, 0
	s_add_i32 m0, s39, 0x1c000
	v_and_b32_e32 v6, 32, v5
	global_load_lds_dwordx4 v2, s[2:3]
	v_mov_b32_e32 v2, v190
	s_add_i32 m0, s39, 0x1e000
	s_cmpk_lt_u32 s6, 0x100
	global_load_lds_dwordx4 v2, s[2:3]
	v_and_b32_e32 v2, 48, v0
	v_or_b32_e32 v4, v3, v2
	v_bitop3_b32 v2, v3, v6, v2 bitop3:0x36
	v_bitop3_b32 v3, s14, v4, v6 bitop3:0xf6
	v_or_b32_e32 v196, s15, v2
	s_cselect_b64 s[14:15], -1, 0
	s_add_i32 s3, 0, 0x27d04
	v_writelane_b32 v255, s3, 55
	s_add_i32 s3, 0, 0x27d4c
	v_writelane_b32 v255, s3, 56
	s_add_i32 s3, 0, 0x27d54
	v_writelane_b32 v255, s3, 57
	s_add_i32 s3, 0, 0x27d5c
	v_writelane_b32 v255, s3, 58
	s_add_i32 s3, 0, 0x27d64
	s_waitcnt vmcnt(0)
	v_writelane_b32 v255, s3, 59
	s_add_i32 s3, 0, 0x27d6c
	s_mov_b32 s4, 0
	s_add_i32 s2, 0, 0x27d80
	v_writelane_b32 v255, s3, 60
	s_add_i32 s3, 0, 0x27d74
	v_mov_b32_e32 v187, 0
	v_add_u32_e32 v197, s60, v5
	s_ashr_i32 s96, s96, 31
	s_add_i32 s9, 0, 0x27d0c
	s_add_i32 s8, 0, 0x27d14
	s_add_i32 s17, 0, 0x27d1c
	s_add_i32 s50, 0, 0x27d24
	s_add_i32 s10, 0, 0x27d2c
	s_add_i32 s11, 0, 0x27d34
	s_add_i32 s56, 0, 0x27d3c
	s_add_i32 s57, 0, 0x27d44
	v_writelane_b32 v255, s3, 61
	s_add_i32 s91, 0, 0x27d7c
	v_lshlrev_b32_e32 v198, 2, v0
	s_add_i32 s92, 0, 0x10000
	s_add_i32 s93, 0, 0x14000
	s_mov_b32 s5, s4
	s_mov_b32 s6, s4
	s_mov_b32 s7, s4
	s_mov_b32 s16, 0xc01d265f
	s_mov_b32 s94, 0xc15083aa
	s_mov_b32 s98, 0xbfd083aa
	v_mov_b32_e32 v199, s2
	v_add_u32_e32 v200, 0, v3
	v_mov_b32_e32 v201, 1
	v_mov_b32_e32 v42, 0xba1d265f
	v_mov_b32_e32 v46, 0xb9d083aa
	v_mov_b32_e32 v202, 0x411c62c0
	v_mov_b32_e32 v188, 0x3fd083aa
	s_mov_b32 s95, s4
	s_mov_b64 s[24:25], s[28:29]
	s_barrier
	v_mov_b32_e32 v4, v0
	s_nop 0
	v_ashrrev_i32_e32 v6, 31, v4
	v_lshrrev_b32_e32 v6, 26, v6
	v_lshlrev_b32_e32 v5, 4, v4
	v_add_u32_e32 v6, v4, v6
	v_bfe_i32 v4, v4, 27, 1
	v_lshrrev_b32_e32 v4, 22, v4
	v_add_u32_e32 v4, v5, v4
	v_and_b32_e32 v4, 0xfffffc00, v4
	v_sub_u32_e32 v4, v5, v4
	v_lshrrev_b32_e32 v7, 4, v4
	v_bitop3_b32 v4, v7, v4, 32 bitop3:0x6c
	v_ashrrev_i32_e32 v7, 31, v4
	v_lshrrev_b32_e32 v7, 26, v7
	v_ashrrev_i32_e32 v6, 6, v6
	v_add_u32_e32 v7, v4, v7
	v_ashrrev_i32_e32 v8, 6, v7
	v_lshlrev_b32_e32 v6, 5, v6
	v_and_b32_e32 v9, 32, v6
	v_and_b32_e32 v10, 0xc0, v7
	v_lshlrev_b32_e32 v7, 2, v8
	v_and_b32_e32 v6, 0xffffffc0, v6
	v_add3_u32 v6, s60, v7, v6
	v_mov_b32_e32 v246, v6
	v_sub_u32_e32 v4, v4, v10
	v_ashrrev_i16_sdwa v4, v201, sext(v4) dst_sel:DWORD dst_unused:UNUSED_PAD src0_sel:DWORD src1_sel:BYTE_0
	v_bfe_i32 v4, v4, 0, 16
	v_add_lshl_u32 v4, v9, v4, 1
	v_mov_b32_e32 v247, v4
	v_add_u32_e32 v4, 0x2000, v5
	v_ashrrev_i32_e32 v5, 31, v4
	v_lshrrev_b32_e32 v5, 22, v5
	v_add_u32_e32 v5, v4, v5
	v_ashrrev_i32_e32 v5, 10, v5
	v_mul_i32_i24_e32 v6, 0x400, v5
	v_sub_u32_e32 v4, v4, v6
	v_lshrrev_b32_e32 v6, 4, v4
	v_bitop3_b32 v4, v6, v4, 32 bitop3:0x6c
	v_ashrrev_i32_e32 v6, 31, v4
	v_lshrrev_b32_e32 v6, 26, v6
	v_add_u32_e32 v6, v4, v6
	v_ashrrev_i32_e32 v7, 6, v6
	v_lshlrev_b32_e32 v5, 5, v5
	v_and_b32_e32 v8, 32, v5
	v_and_b32_e32 v9, 0xc0, v6
	v_lshlrev_b32_e32 v6, 2, v7
	v_and_b32_e32 v5, 0xffffffc0, v5
	v_add3_u32 v5, s60, v6, v5
	v_mov_b32_e32 v248, v5
	v_sub_u32_e32 v4, v4, v9
	v_ashrrev_i16_sdwa v4, v201, sext(v4) dst_sel:DWORD dst_unused:UNUSED_PAD src0_sel:DWORD src1_sel:BYTE_0
	v_bfe_i32 v4, v4, 0, 16
	v_add_lshl_u32 v4, v8, v4, 1
	v_mov_b32_e32 v249, v4
	s_branch .LBB0_727

; __device__ __forceinline__ unsigned pk4_fp8(float a, float b, float c, float d) { int v = 0; v = __builtin_amdgcn_cvt_pk_fp8_f32(a, b, v, false); v = __builtin_amdgcn_cvt_pk_fp8_f32(c, d, v, true); return (unsigned)v; }
;     __device__ __forceinline__ void operator()(const f32x4 (&acc)[2][2][4][2], const pg8::Unit& u, const Pre& q, int wr, int wc, int fr, int fq) const {
;         const int row0 = u.pm * 256 + wr * 64 + fr, f0w = u.pn * 128 + wc * 32;
;         constexpr float DS = 1.0f / (FP8_SA * FP8_SW);
;         f32x4 dsk = (f32x4){DS * KP, DS * KP, DS * KP, DS * KP}, dsu = (f32x4){DS, DS, DS, DS}; asm volatile("" : "+v"(dsk), "+v"(dsu));
; #pragma unroll
;         for (int ai = 0; ai < 2; ++ai)
; #pragma unroll
;             for (int mp = 0; mp < 2; ++mp) { unsigned lo[2], hi[2];
; #pragma unroll
;                 for (int mm = 0; mm < 2; ++mm) { const int m = 2 * mp + mm; float h[8];
; #pragma unroll
;                     for (int n = 0; n < 2; ++n) { const f32x4 gk = __builtin_elementwise_fma(acc[ai][0][m][n], dsk, q.bg[n]), up = __builtin_elementwise_fma(acc[ai][1][m][n], dsu, q.bu[n]);
; #pragma unroll
;                         for (int j = 0; j < 4; ++j) { const float gm = __builtin_fmaxf(gk[j], 7.0f * KP), li = __builtin_amdgcn_fmed3f(up[j], -7.0f, 7.0f);
;                             const float sg = __builtin_amdgcn_rcpf(1.0f + __builtin_amdgcn_exp2f(gm));
;                             h[n * 4 + j] = (gm * sg) * (li * (FP8_SH / KP) + (FP8_SH / KP)); } }
;                     lo[mm] = pk4_fp8(h[0], h[1], h[2], h[3]); hi[mm] = pk4_fp8(h[4], h[5], h[6], h[7]); }
.LBB0_739:
	v_mov_b32_e32 v11, v0
	v_mov_b32_e32 v43, v42
	v_readfirstlane_b32 s19, v11
	v_mov_b32_e32 v47, v46
	s_ashr_i32 s27, s19, 2
	v_mov_b32_e32 v44, v42
	v_mov_b32_e32 v45, v42
	v_mov_b32_e32 v48, v46
	v_mov_b32_e32 v49, v46
	v_pk_fma_f32 v[38:39], v[38:39], s[98:99], s[98:99] op_sel_hi:[1,0,0]
	v_pk_fma_f32 v[40:41], v[40:41], s[98:99], s[98:99] op_sel_hi:[1,0,0]
	v_pk_fma_f32 v[34:35], v[34:35], s[98:99], s[98:99] op_sel_hi:[1,0,0]
	v_pk_fma_f32 v[36:37], v[36:37], s[98:99], s[98:99] op_sel_hi:[1,0,0]
	v_mov_b64_e32 v[2:3], v[46:47]
	v_mov_b64_e32 v[6:7], v[42:43]
	v_pk_mul_f32 v[18:19], v[78:79], s[16:17] op_sel_hi:[1,0]
	s_lshl_b32 s21, s38, 8
	s_andn2_b32 s27, s27, 63
	v_mov_b64_e32 v[4:5], v[48:49]
	v_mov_b64_e32 v[8:9], v[44:45]
	s_add_i32 s27, s27, s21
	v_and_or_b32 v10, v11, 31, s27
	v_pk_fma_f32 v[20:21], v[178:179], v[6:7], v[18:19]
	v_lshrrev_b32_e32 v11, 1, v11
	v_max_f32_e32 v23, 0xc1898193, v20
	v_and_b32_e32 v186, 16, v11
	v_exp_f32_e32 v11, v23
	v_max_f32_e32 v21, 0xc1898193, v21
	v_pk_fma_f32 v[28:29], v[182:183], v[2:3], v[38:39]
	v_pk_mul_f32 v[16:17], v[80:81], s[16:17] op_sel_hi:[1,0]
	v_add_f32_e32 v11, 1.0, v11
	v_rcp_f32_e32 v189, v11
	v_exp_f32_e32 v11, v21
	v_med3_f32 v22, v28, s94, v202
	v_pk_fma_f32 v[24:25], v[180:181], v[8:9], v[16:17]
	v_mul_f32_e32 v23, v23, v189
	v_add_f32_e32 v11, 1.0, v11
	v_mul_f32_e32 v30, v22, v23
	v_max_f32_e32 v23, 0xc1898193, v24
	v_rcp_f32_e32 v189, v11
	v_exp_f32_e32 v11, v23
	v_med3_f32 v20, v29, s94, v202
	v_max_f32_e32 v25, 0xc1898193, v25
	v_mul_f32_e32 v21, v21, v189
	v_add_f32_e32 v11, 1.0, v11
	v_rcp_f32_e32 v189, v11
	v_exp_f32_e32 v11, v25
	v_pk_fma_f32 v[26:27], v[184:185], v[4:5], v[40:41]
	v_med3_f32 v22, v26, s94, v202
	v_add_f32_e32 v11, 1.0, v11
	v_mul_f32_e32 v31, v20, v21
	v_mul_f32_e32 v21, v23, v189
	v_rcp_f32_e32 v189, v11
	v_med3_f32 v24, v27, s94, v202
	v_mul_f32_e32 v11, v22, v21
	v_mul_f32_e32 v21, v25, v189
	v_pk_mul_f32 v[14:15], v[74:75], s[16:17] op_sel_hi:[1,0]
	v_mul_f32_e32 v32, v24, v21
	v_pk_fma_f32 v[20:21], v[170:171], v[6:7], v[14:15]
	v_pk_fma_f32 v[28:29], v[174:175], v[2:3], v[34:35]
	v_max_f32_e32 v23, 0xc1898193, v20
	v_exp_f32_e32 v20, v23
	v_max_f32_e32 v21, 0xc1898193, v21
	v_med3_f32 v22, v28, s94, v202
	v_pk_mul_f32 v[12:13], v[76:77], s[16:17] op_sel_hi:[1,0]
	v_add_f32_e32 v20, 1.0, v20
	v_rcp_f32_e32 v189, v20
	v_exp_f32_e32 v20, v21
	v_pk_fma_f32 v[24:25], v[172:173], v[8:9], v[12:13]
	v_pk_fma_f32 v[26:27], v[176:177], v[4:5], v[36:37]
	v_mul_f32_e32 v23, v23, v189
	v_add_f32_e32 v20, 1.0, v20
	v_mul_f32_e32 v28, v22, v23
	v_max_f32_e32 v23, 0xc1898193, v24
	v_exp_f32_e32 v22, v23
	v_rcp_f32_e32 v189, v20
	v_med3_f32 v20, v29, s94, v202
	v_max_f32_e32 v25, 0xc1898193, v25
	v_add_f32_e32 v22, 1.0, v22
	v_mul_f32_e32 v21, v21, v189
	v_rcp_f32_e32 v189, v22
	v_exp_f32_e32 v24, v25
	v_med3_f32 v22, v26, s94, v202
	v_mul_f32_e32 v29, v20, v21
	v_mul_f32_e32 v21, v23, v189
	v_mov_b32_e32 v20, v22
	v_add_f32_e32 v22, 1.0, v24
	v_rcp_f32_e32 v189, v22
	v_mul_f32_e32 v26, v20, v21
	v_mov_b32_e32 v21, v187
	v_med3_f32 v24, v27, s94, v202
	v_cvt_pk_fp8_f32 v21, v28, v29
	v_mul_f32_e32 v23, v25, v189
	v_mov_b32_e32 v20, v187
	v_cvt_pk_fp8_f32 v20, v30, v31
	v_mul_f32_e32 v22, v24, v23
	v_cvt_pk_fp8_f32 v21, v26, v22 op_sel:[0,0,1]
	v_pk_fma_f32 v[22:23], v[162:163], v[6:7], v[18:19]
	v_cvt_pk_fp8_f32 v20, v11, v32 op_sel:[0,0,1]
	v_max_f32_e32 v25, 0xc1898193, v22
	v_exp_f32_e32 v11, v25
	v_max_f32_e32 v23, 0xc1898193, v23
	v_pk_fma_f32 v[30:31], v[166:167], v[2:3], v[38:39]
	v_pk_fma_f32 v[26:27], v[164:165], v[8:9], v[16:17]
	v_add_f32_e32 v11, 1.0, v11
	v_rcp_f32_e32 v189, v11
	v_exp_f32_e32 v11, v23
	v_med3_f32 v24, v30, s94, v202
	v_max_f32_e32 v27, 0xc1898193, v27
	v_mul_f32_e32 v25, v25, v189
	v_add_f32_e32 v11, 1.0, v11
	v_mul_f32_e32 v32, v24, v25
	v_max_f32_e32 v25, 0xc1898193, v26
	v_rcp_f32_e32 v189, v11
	v_exp_f32_e32 v11, v25
	v_med3_f32 v22, v31, s94, v202
	v_pk_fma_f32 v[28:29], v[168:169], v[4:5], v[40:41]
	v_mul_f32_e32 v23, v23, v189
	v_add_f32_e32 v11, 1.0, v11
	v_rcp_f32_e32 v189, v11
	v_exp_f32_e32 v11, v27
	v_med3_f32 v24, v28, s94, v202
	v_mul_f32_e32 v33, v22, v23
	v_add_f32_e32 v11, 1.0, v11
	v_mul_f32_e32 v23, v25, v189
	v_rcp_f32_e32 v189, v11
	v_med3_f32 v26, v29, s94, v202
	v_mul_f32_e32 v11, v24, v23
	v_mul_f32_e32 v23, v27, v189
	v_pk_fma_f32 v[30:31], v[158:159], v[2:3], v[34:35]
	v_mul_f32_e32 v43, v26, v23
	v_pk_fma_f32 v[22:23], v[154:155], v[6:7], v[14:15]
	v_med3_f32 v24, v30, s94, v202
	v_max_f32_e32 v25, 0xc1898193, v22
	v_exp_f32_e32 v22, v25
	v_max_f32_e32 v23, 0xc1898193, v23
	v_pk_fma_f32 v[26:27], v[156:157], v[8:9], v[12:13]
	v_pk_fma_f32 v[28:29], v[160:161], v[4:5], v[36:37]
	v_add_f32_e32 v22, 1.0, v22
	v_rcp_f32_e32 v189, v22
	v_exp_f32_e32 v22, v23
	v_max_f32_e32 v27, 0xc1898193, v27
	s_lshr_b32 s19, s19, 1
	v_mul_f32_e32 v25, v25, v189
	v_add_f32_e32 v22, 1.0, v22
	v_mul_f32_e32 v30, v24, v25
	v_max_f32_e32 v25, 0xc1898193, v26
	v_exp_f32_e32 v24, v25
	v_rcp_f32_e32 v189, v22
	v_med3_f32 v22, v31, s94, v202
	v_exp_f32_e32 v26, v27
	v_add_f32_e32 v24, 1.0, v24
	v_mul_f32_e32 v23, v23, v189
	v_rcp_f32_e32 v189, v24
	v_med3_f32 v24, v28, s94, v202
	v_mul_f32_e32 v31, v22, v23
	v_mul_f32_e32 v23, v25, v189
	v_mov_b32_e32 v22, v24
	v_add_f32_e32 v24, 1.0, v26
	v_rcp_f32_e32 v189, v24
	v_mul_f32_e32 v28, v22, v23
	v_mov_b32_e32 v22, v187
	v_cvt_pk_fp8_f32 v22, v32, v33
	v_mov_b32_e32 v23, v187
	v_med3_f32 v26, v29, s94, v202
	v_cvt_pk_fp8_f32 v23, v30, v31
	v_mul_f32_e32 v25, v27, v189
	v_cvt_pk_fp8_f32 v22, v11, v43 op_sel:[0,0,1]
	v_mul_f32_e32 v11, v26, v25
	s_lshl_b32 s21, s26, 7
; __device__ __forceinline__ unsigned pk4_fp8(float a, float b, float c, float d) { int v = 0; v = __builtin_amdgcn_cvt_pk_fp8_f32(a, b, v, false); v = __builtin_amdgcn_cvt_pk_fp8_f32(c, d, v, true); return (unsigned)v; }
;     __device__ __forceinline__ void operator()(const f32x4 (&acc)[2][2][4][2], const pg8::Unit& u, const Pre& q, int wr, int wc, int fr, int fq) const {
;         const int row0 = u.pm * 256 + wr * 64 + fr, f0w = u.pn * 128 + wc * 32;
;         constexpr float DS = 1.0f / (FP8_SA * FP8_SW);
;         f32x4 dsk = (f32x4){DS * KP, DS * KP, DS * KP, DS * KP}, dsu = (f32x4){DS, DS, DS, DS}; asm volatile("" : "+v"(dsk), "+v"(dsu));
; #pragma unroll
;         for (int ai = 0; ai < 2; ++ai)
; #pragma unroll
;             for (int mp = 0; mp < 2; ++mp) { unsigned lo[2], hi[2];
; #pragma unroll
;                 for (int mm = 0; mm < 2; ++mm) { const int m = 2 * mp + mm; float h[8];
; #pragma unroll
;                     for (int n = 0; n < 2; ++n) { const f32x4 gk = __builtin_elementwise_fma(acc[ai][0][m][n], dsk, q.bg[n]), up = __builtin_elementwise_fma(acc[ai][1][m][n], dsu, q.bu[n]);
; #pragma unroll
;                         for (int j = 0; j < 4; ++j) { const float gm = __builtin_fmaxf(gk[j], 7.0f * KP), li = __builtin_amdgcn_fmed3f(up[j], -7.0f, 7.0f);
;                             const float sg = __builtin_amdgcn_rcpf(1.0f + __builtin_amdgcn_exp2f(gm));
;                             h[n * 4 + j] = (gm * sg) * (li * (FP8_SH / KP) + (FP8_SH / KP)); } }
;                     lo[mm] = pk4_fp8(h[0], h[1], h[2], h[3]); hi[mm] = pk4_fp8(h[4], h[5], h[6], h[7]); }
;                 const v2u r0 = __builtin_amdgcn_permlane16_swap(lo[0], lo[1], false, false), r1 = __builtin_amdgcn_permlane16_swap(hi[0], hi[1], false, false);
;                 unsigned char* rowp = hb + (size_t)(row0 + ai * 128 + (2 * mp + (fq & 1)) * 16) * FF + f0w + 16 * (fq >> 1);
;                 *(v4u*)rowp = (v4u){r0.x, r1.x, r0.y, r1.y}; }
;     }
	s_and_b32 s19, s19, 0x60
	v_cvt_pk_fp8_f32 v23, v28, v11 op_sel:[0,0,1]
	v_ashrrev_i32_e32 v11, 31, v10
	s_or_b32 s26, s19, s21
	v_lshlrev_b64 v[24:25], 11, v[10:11]
	s_ashr_i32 s27, s26, 31
	v_lshl_add_u64 v[24:25], s[12:13], 0, v[24:25]
	v_lshl_add_u64 v[24:25], v[24:25], 0, s[26:27]
	v_permlane16_swap_b32_e32 v20, v22
	v_permlane16_swap_b32_e32 v21, v23
	v_lshl_add_u64 v[24:25], v[24:25], 0, v[186:187]
	global_store_dwordx4 v[24:25], v[20:23], off
	v_pk_fma_f32 v[28:29], v[150:151], v[2:3], v[38:39]
	v_pk_fma_f32 v[24:25], v[148:149], v[8:9], v[16:17]
	v_pk_fma_f32 v[20:21], v[146:147], v[6:7], v[18:19]
	v_med3_f32 v22, v28, s94, v202
	v_max_f32_e32 v23, 0xc1898193, v20
	v_exp_f32_e32 v11, v23
	v_max_f32_e32 v21, 0xc1898193, v21
	v_max_f32_e32 v25, 0xc1898193, v25
	v_pk_fma_f32 v[26:27], v[152:153], v[4:5], v[40:41]
	v_add_f32_e32 v11, 1.0, v11
	v_rcp_f32_e32 v189, v11
	v_exp_f32_e32 v11, v21
	s_andn2_b64 vcc, exec, s[2:3]
	s_mov_b64 s[2:3], -1
	v_mul_f32_e32 v23, v23, v189
	v_add_f32_e32 v11, 1.0, v11
	v_mul_f32_e32 v30, v22, v23
	v_max_f32_e32 v23, 0xc1898193, v24
	v_rcp_f32_e32 v189, v11
	v_exp_f32_e32 v11, v23
	v_med3_f32 v20, v29, s94, v202
	v_med3_f32 v22, v26, s94, v202
	v_mul_f32_e32 v21, v21, v189
	v_add_f32_e32 v11, 1.0, v11
	v_rcp_f32_e32 v189, v11
	v_exp_f32_e32 v11, v25
	v_mul_f32_e32 v31, v20, v21
	v_mul_f32_e32 v21, v23, v189
	v_add_f32_e32 v11, 1.0, v11
	v_rcp_f32_e32 v189, v11
	v_med3_f32 v24, v27, s94, v202
	v_mul_f32_e32 v11, v22, v21
	v_mul_f32_e32 v21, v25, v189
	v_pk_fma_f32 v[28:29], v[142:143], v[2:3], v[34:35]
	v_mul_f32_e32 v32, v24, v21
	v_pk_fma_f32 v[20:21], v[138:139], v[6:7], v[14:15]
	v_med3_f32 v22, v28, s94, v202
	v_max_f32_e32 v23, 0xc1898193, v20
	v_exp_f32_e32 v20, v23
	v_max_f32_e32 v21, 0xc1898193, v21
	v_pk_fma_f32 v[24:25], v[140:141], v[8:9], v[12:13]
	v_pk_fma_f32 v[26:27], v[144:145], v[4:5], v[36:37]
	v_add_f32_e32 v20, 1.0, v20
	v_rcp_f32_e32 v189, v20
	v_exp_f32_e32 v20, v21
	v_max_f32_e32 v25, 0xc1898193, v25
	v_mul_f32_e32 v23, v23, v189
	s_nop 0
	v_mul_f32_e32 v28, v22, v23
	v_max_f32_e32 v23, 0xc1898193, v24
	v_add_f32_e32 v20, 1.0, v20
	v_exp_f32_e32 v22, v23
	v_rcp_f32_e32 v189, v20
	v_med3_f32 v20, v29, s94, v202
	v_exp_f32_e32 v24, v25
	v_add_f32_e32 v22, 1.0, v22
	v_mul_f32_e32 v21, v21, v189
	v_rcp_f32_e32 v189, v22
	v_med3_f32 v22, v26, s94, v202
	v_mul_f32_e32 v29, v20, v21
	v_mul_f32_e32 v21, v23, v189
	v_mov_b32_e32 v20, v22
	v_add_f32_e32 v22, 1.0, v24
	v_rcp_f32_e32 v189, v22
	v_mul_f32_e32 v26, v20, v21
	v_mov_b32_e32 v21, v187
	v_med3_f32 v24, v27, s94, v202
	v_cvt_pk_fp8_f32 v21, v28, v29
	v_mul_f32_e32 v23, v25, v189
	v_mov_b32_e32 v20, v187
	v_cvt_pk_fp8_f32 v20, v30, v31
	v_mul_f32_e32 v22, v24, v23
	v_cvt_pk_fp8_f32 v21, v26, v22 op_sel:[0,0,1]
	v_pk_fma_f32 v[22:23], v[130:131], v[6:7], v[18:19]
	v_cvt_pk_fp8_f32 v20, v11, v32 op_sel:[0,0,1]
	v_max_f32_e32 v25, 0xc1898193, v22
	v_exp_f32_e32 v11, v25
	v_max_f32_e32 v23, 0xc1898193, v23
	v_pk_fma_f32 v[30:31], v[134:135], v[2:3], v[38:39]
	v_pk_fma_f32 v[26:27], v[132:133], v[8:9], v[16:17]
	v_add_f32_e32 v11, 1.0, v11
	v_rcp_f32_e32 v189, v11
	v_exp_f32_e32 v11, v23
	v_med3_f32 v24, v30, s94, v202
	v_max_f32_e32 v27, 0xc1898193, v27
	v_mul_f32_e32 v25, v25, v189
	v_add_f32_e32 v11, 1.0, v11
	v_mul_f32_e32 v32, v24, v25
	v_max_f32_e32 v25, 0xc1898193, v26
	v_rcp_f32_e32 v189, v11
	v_exp_f32_e32 v11, v25
	v_med3_f32 v22, v31, s94, v202
	v_pk_fma_f32 v[28:29], v[136:137], v[4:5], v[40:41]
	v_mul_f32_e32 v23, v23, v189
	v_add_f32_e32 v11, 1.0, v11
	v_rcp_f32_e32 v189, v11
	v_exp_f32_e32 v11, v27
	v_med3_f32 v24, v28, s94, v202
	v_mul_f32_e32 v33, v22, v23
	v_add_f32_e32 v11, 1.0, v11
	v_mul_f32_e32 v23, v25, v189
	v_rcp_f32_e32 v189, v11
	v_med3_f32 v26, v29, s94, v202
	v_mul_f32_e32 v11, v24, v23
	v_mul_f32_e32 v23, v27, v189
	v_pk_fma_f32 v[30:31], v[126:127], v[2:3], v[34:35]
	v_mul_f32_e32 v43, v26, v23
	v_pk_fma_f32 v[22:23], v[122:123], v[6:7], v[14:15]
	v_med3_f32 v24, v30, s94, v202
	v_max_f32_e32 v25, 0xc1898193, v22
	v_exp_f32_e32 v22, v25
	v_max_f32_e32 v23, 0xc1898193, v23
	v_pk_fma_f32 v[26:27], v[124:125], v[8:9], v[12:13]
	v_pk_fma_f32 v[28:29], v[128:129], v[4:5], v[36:37]
	v_add_f32_e32 v22, 1.0, v22
	v_rcp_f32_e32 v189, v22
	v_exp_f32_e32 v22, v23
	v_max_f32_e32 v27, 0xc1898193, v27
	v_mul_f32_e32 v25, v25, v189
	s_nop 0
	v_mul_f32_e32 v30, v24, v25
	v_max_f32_e32 v25, 0xc1898193, v26
	v_add_f32_e32 v22, 1.0, v22
	v_exp_f32_e32 v24, v25
	v_rcp_f32_e32 v189, v22
	v_med3_f32 v22, v31, s94, v202
	v_exp_f32_e32 v26, v27
	v_add_f32_e32 v24, 1.0, v24
	v_mul_f32_e32 v23, v23, v189
	v_rcp_f32_e32 v189, v24
	v_med3_f32 v24, v28, s94, v202
	v_mul_f32_e32 v31, v22, v23
	v_mul_f32_e32 v23, v25, v189
	v_mov_b32_e32 v22, v24
	v_add_f32_e32 v24, 1.0, v26
	v_rcp_f32_e32 v189, v24
	v_mul_f32_e32 v28, v22, v23
	v_mov_b32_e32 v22, v187
	v_cvt_pk_fp8_f32 v22, v32, v33
	v_mov_b32_e32 v23, v187
	v_med3_f32 v26, v29, s94, v202
	v_cvt_pk_fp8_f32 v23, v30, v31
	v_mul_f32_e32 v25, v27, v189
	v_cvt_pk_fp8_f32 v22, v11, v43 op_sel:[0,0,1]
	v_mul_f32_e32 v11, v26, v25
	v_or_b32_e32 v24, 32, v10
	v_cvt_pk_fp8_f32 v23, v28, v11 op_sel:[0,0,1]
	v_ashrrev_i32_e32 v25, 31, v24
	v_lshlrev_b64 v[24:25], 11, v[24:25]
	v_lshl_add_u64 v[24:25], s[12:13], 0, v[24:25]
	v_lshl_add_u64 v[24:25], v[24:25], 0, s[26:27]
	v_permlane16_swap_b32_e32 v20, v22
	v_permlane16_swap_b32_e32 v21, v23
	v_lshl_add_u64 v[24:25], v[24:25], 0, v[186:187]
	global_store_dwordx4 v[24:25], v[20:23], off
	v_pk_fma_f32 v[30:31], v[106:107], v[2:3], v[38:39]
	v_pk_fma_f32 v[26:27], v[120:121], v[8:9], v[16:17]
	v_pk_fma_f32 v[22:23], v[118:119], v[6:7], v[18:19]
; __device__ __forceinline__ unsigned pk4_fp8(float a, float b, float c, float d) { int v = 0; v = __builtin_amdgcn_cvt_pk_fp8_f32(a, b, v, false); v = __builtin_amdgcn_cvt_pk_fp8_f32(c, d, v, true); return (unsigned)v; }
;     __device__ __forceinline__ void operator()(const f32x4 (&acc)[2][2][4][2], const pg8::Unit& u, const Pre& q, int wr, int wc, int fr, int fq) const {
;         const int row0 = u.pm * 256 + wr * 64 + fr, f0w = u.pn * 128 + wc * 32;
;         constexpr float DS = 1.0f / (FP8_SA * FP8_SW);
;         f32x4 dsk = (f32x4){DS * KP, DS * KP, DS * KP, DS * KP}, dsu = (f32x4){DS, DS, DS, DS}; asm volatile("" : "+v"(dsk), "+v"(dsu));
; #pragma unroll
;         for (int ai = 0; ai < 2; ++ai)
; #pragma unroll
;             for (int mp = 0; mp < 2; ++mp) { unsigned lo[2], hi[2];
; #pragma unroll
;                 for (int mm = 0; mm < 2; ++mm) { const int m = 2 * mp + mm; float h[8];
; #pragma unroll
;                     for (int n = 0; n < 2; ++n) { const f32x4 gk = __builtin_elementwise_fma(acc[ai][0][m][n], dsk, q.bg[n]), up = __builtin_elementwise_fma(acc[ai][1][m][n], dsu, q.bu[n]);
; #pragma unroll
;                         for (int j = 0; j < 4; ++j) { const float gm = __builtin_fmaxf(gk[j], 7.0f * KP), li = __builtin_amdgcn_fmed3f(up[j], -7.0f, 7.0f);
;                             const float sg = __builtin_amdgcn_rcpf(1.0f + __builtin_amdgcn_exp2f(gm));
;                             h[n * 4 + j] = (gm * sg) * (li * (FP8_SH / KP) + (FP8_SH / KP)); } }
;                     lo[mm] = pk4_fp8(h[0], h[1], h[2], h[3]); hi[mm] = pk4_fp8(h[4], h[5], h[6], h[7]); }
;                 const v2u r0 = __builtin_amdgcn_permlane16_swap(lo[0], lo[1], false, false), r1 = __builtin_amdgcn_permlane16_swap(hi[0], hi[1], false, false);
;                 unsigned char* rowp = hb + (size_t)(row0 + ai * 128 + (2 * mp + (fq & 1)) * 16) * FF + f0w + 16 * (fq >> 1);
;                 *(v4u*)rowp = (v4u){r0.x, r1.x, r0.y, r1.y}; }
;     }
	v_med3_f32 v24, v30, s94, v202
	v_max_f32_e32 v25, 0xc1898193, v22
	v_exp_f32_e32 v11, v25
	v_max_f32_e32 v23, 0xc1898193, v23
	v_med3_f32 v22, v31, s94, v202
	v_max_f32_e32 v27, 0xc1898193, v27
	v_add_f32_e32 v11, 1.0, v11
	v_rcp_f32_e32 v189, v11
	v_exp_f32_e32 v11, v23
	v_pk_fma_f32 v[28:29], v[108:109], v[4:5], v[40:41]
	v_pk_fma_f32 v[30:31], v[114:115], v[2:3], v[34:35]
	v_mul_f32_e32 v25, v25, v189
	v_add_f32_e32 v11, 1.0, v11
	v_mul_f32_e32 v21, v24, v25
	v_max_f32_e32 v25, 0xc1898193, v26
	v_rcp_f32_e32 v189, v11
	v_exp_f32_e32 v11, v25
	v_med3_f32 v24, v28, s94, v202
	v_med3_f32 v26, v29, s94, v202
	v_mul_f32_e32 v23, v23, v189
	v_add_f32_e32 v11, 1.0, v11
	v_rcp_f32_e32 v189, v11
	v_exp_f32_e32 v11, v27
	v_mul_f32_e32 v32, v22, v23
	v_mul_f32_e32 v23, v25, v189
	v_add_f32_e32 v11, 1.0, v11
	v_rcp_f32_e32 v189, v11
	v_mul_f32_e32 v11, v24, v23
	v_med3_f32 v24, v30, s94, v202
	v_mul_f32_e32 v23, v27, v189
	v_mov_b32_e32 v22, v26
	v_pk_fma_f32 v[26:27], v[112:113], v[8:9], v[12:13]
	v_mul_f32_e32 v33, v22, v23
	v_pk_fma_f32 v[22:23], v[110:111], v[6:7], v[14:15]
	v_max_f32_e32 v27, 0xc1898193, v27
	v_max_f32_e32 v25, 0xc1898193, v22
	v_exp_f32_e32 v22, v25
	v_max_f32_e32 v23, 0xc1898193, v23
	v_pk_fma_f32 v[28:29], v[116:117], v[4:5], v[36:37]
	v_add_u32_e32 v20, 0x80, v10
	v_add_f32_e32 v22, 1.0, v22
	v_rcp_f32_e32 v189, v22
	v_exp_f32_e32 v22, v23
	v_mul_f32_e32 v25, v25, v189
	s_nop 0
	v_mul_f32_e32 v30, v24, v25
	v_max_f32_e32 v25, 0xc1898193, v26
	v_add_f32_e32 v22, 1.0, v22
	v_exp_f32_e32 v24, v25
	v_rcp_f32_e32 v189, v22
	v_med3_f32 v22, v31, s94, v202
	v_exp_f32_e32 v26, v27
	v_add_f32_e32 v24, 1.0, v24
	v_mul_f32_e32 v23, v23, v189
	v_rcp_f32_e32 v189, v24
	v_med3_f32 v24, v28, s94, v202
	v_mul_f32_e32 v31, v22, v23
	v_mul_f32_e32 v23, v25, v189
	v_mov_b32_e32 v22, v24
	v_add_f32_e32 v24, 1.0, v26
	v_rcp_f32_e32 v189, v24
	v_mul_f32_e32 v28, v22, v23
	v_med3_f32 v26, v29, s94, v202
	v_mov_b32_e32 v22, v187
	v_mul_f32_e32 v25, v27, v189
	v_cvt_pk_fp8_f32 v22, v21, v32
	v_mul_f32_e32 v21, v26, v25
	v_pk_fma_f32 v[24:25], v[98:99], v[6:7], v[18:19]
	v_cvt_pk_fp8_f32 v22, v11, v33 op_sel:[0,0,1]
	v_max_f32_e32 v27, 0xc1898193, v24
	v_exp_f32_e32 v11, v27
	v_mov_b32_e32 v23, v187
	v_cvt_pk_fp8_f32 v23, v30, v31
	v_max_f32_e32 v25, 0xc1898193, v25
	v_add_f32_e32 v11, 1.0, v11
	v_rcp_f32_e32 v189, v11
	v_pk_fma_f32 v[32:33], v[102:103], v[2:3], v[38:39]
	v_exp_f32_e32 v11, v25
	v_med3_f32 v26, v32, s94, v202
	v_mul_f32_e32 v27, v27, v189
	v_cvt_pk_fp8_f32 v23, v28, v21 op_sel:[0,0,1]
	v_pk_fma_f32 v[28:29], v[100:101], v[8:9], v[16:17]
	v_mul_f32_e32 v21, v26, v27
	v_add_f32_e32 v11, 1.0, v11
	v_max_f32_e32 v27, 0xc1898193, v28
	v_rcp_f32_e32 v189, v11
	v_exp_f32_e32 v11, v27
	v_med3_f32 v24, v33, s94, v202
	v_max_f32_e32 v29, 0xc1898193, v29
	v_mul_f32_e32 v25, v25, v189
	v_add_f32_e32 v11, 1.0, v11
	v_rcp_f32_e32 v189, v11
	v_exp_f32_e32 v11, v29
	v_pk_fma_f32 v[30:31], v[104:105], v[4:5], v[40:41]
	v_med3_f32 v26, v30, s94, v202
	v_add_f32_e32 v11, 1.0, v11
	v_mul_f32_e32 v43, v24, v25
	v_mul_f32_e32 v25, v27, v189
	v_rcp_f32_e32 v189, v11
	v_med3_f32 v28, v31, s94, v202
	v_mul_f32_e32 v11, v26, v25
	v_mul_f32_e32 v25, v29, v189
	v_pk_fma_f32 v[32:33], v[94:95], v[2:3], v[34:35]
	v_mul_f32_e32 v44, v28, v25
	v_pk_fma_f32 v[24:25], v[90:91], v[6:7], v[14:15]
	v_med3_f32 v26, v32, s94, v202
	v_max_f32_e32 v27, 0xc1898193, v24
	v_exp_f32_e32 v24, v27
	v_max_f32_e32 v25, 0xc1898193, v25
	v_pk_fma_f32 v[28:29], v[92:93], v[8:9], v[12:13]
	v_pk_fma_f32 v[30:31], v[96:97], v[4:5], v[36:37]
	v_add_f32_e32 v24, 1.0, v24
	v_rcp_f32_e32 v189, v24
	v_exp_f32_e32 v24, v25
	v_max_f32_e32 v29, 0xc1898193, v29
	v_mul_f32_e32 v27, v27, v189
	s_nop 0
	v_mul_f32_e32 v32, v26, v27
	v_max_f32_e32 v27, 0xc1898193, v28
	v_add_f32_e32 v24, 1.0, v24
	v_exp_f32_e32 v26, v27
	v_rcp_f32_e32 v189, v24
	v_med3_f32 v24, v33, s94, v202
	v_exp_f32_e32 v28, v29
	v_add_f32_e32 v26, 1.0, v26
	v_mul_f32_e32 v25, v25, v189
	v_rcp_f32_e32 v189, v26
	v_med3_f32 v26, v30, s94, v202
	v_mul_f32_e32 v33, v24, v25
	v_mul_f32_e32 v25, v27, v189
	v_mov_b32_e32 v24, v26
	v_add_f32_e32 v26, 1.0, v28
	v_rcp_f32_e32 v189, v26
	v_mul_f32_e32 v30, v24, v25
	v_mov_b32_e32 v24, v187
	v_cvt_pk_fp8_f32 v24, v21, v43
	v_mov_b32_e32 v25, v187
	v_med3_f32 v28, v31, s94, v202
	v_cvt_pk_fp8_f32 v25, v32, v33
	v_mul_f32_e32 v27, v29, v189
	v_cvt_pk_fp8_f32 v24, v11, v44 op_sel:[0,0,1]
	v_mul_f32_e32 v11, v28, v27
	v_cvt_pk_fp8_f32 v25, v30, v11 op_sel:[0,0,1]
	v_ashrrev_i32_e32 v21, 31, v20
	v_lshlrev_b64 v[20:21], 11, v[20:21]
	v_lshl_add_u64 v[20:21], s[12:13], 0, v[20:21]
	v_lshl_add_u64 v[20:21], v[20:21], 0, s[26:27]
	v_permlane16_swap_b32_e32 v22, v24
	v_permlane16_swap_b32_e32 v23, v25
	v_lshl_add_u64 v[20:21], v[20:21], 0, v[186:187]
	global_store_dwordx4 v[20:21], v[22:25], off
	v_pk_fma_f32 v[20:21], v[82:83], v[6:7], v[18:19]
	v_pk_fma_f32 v[28:29], v[86:87], v[2:3], v[38:39]
	v_max_f32_e32 v23, 0xc1898193, v20
	v_exp_f32_e32 v11, v23
	v_max_f32_e32 v21, 0xc1898193, v21
	v_med3_f32 v22, v28, s94, v202
	v_pk_fma_f32 v[24:25], v[84:85], v[8:9], v[16:17]
	v_add_f32_e32 v11, 1.0, v11
	v_rcp_f32_e32 v189, v11
	v_exp_f32_e32 v11, v21
	v_max_f32_e32 v25, 0xc1898193, v25
	v_pk_fma_f32 v[26:27], v[88:89], v[4:5], v[40:41]
	v_mul_f32_e32 v23, v23, v189
	v_add_f32_e32 v11, 1.0, v11
	v_mul_f32_e32 v30, v22, v23
	v_max_f32_e32 v23, 0xc1898193, v24
	v_rcp_f32_e32 v189, v11
	v_exp_f32_e32 v11, v23
	v_med3_f32 v20, v29, s94, v202
; __device__ __forceinline__ unsigned pk4_fp8(float a, float b, float c, float d) { int v = 0; v = __builtin_amdgcn_cvt_pk_fp8_f32(a, b, v, false); v = __builtin_amdgcn_cvt_pk_fp8_f32(c, d, v, true); return (unsigned)v; }
;     __device__ __forceinline__ void prefetch(const pg8::Unit& u, Pre& q) const {
;         int tz = threadIdx.x; asm volatile("" : "+v"(tz)); const int wc = (tz >> 6) & 3, fq = (tz >> 4) & 3;
;         const int f0 = u.pn * 128 + wc * 32 + 8 * fq;
; #pragma unroll
;         for (int n = 0; n < 2; ++n) { q.bg[n] = *(const f32x4*)(b_gate + (size_t)u.e * FF + f0 + 4 * n) * KP; q.bu[n] = *(const f32x4*)(b_up + (size_t)u.e * FF + f0 + 4 * n); }
;     __device__ __forceinline__ void operator()(const f32x4 (&acc)[2][2][4][2], const pg8::Unit& u, const Pre& q, int wr, int wc, int fr, int fq) const {
;     ...
;             for (int mp = 0; mp < 2; ++mp) { unsigned lo[2], hi[2];
; #pragma unroll
;                 for (int mm = 0; mm < 2; ++mm) { const int m = 2 * mp + mm; float h[8];
; #pragma unroll
;                     for (int n = 0; n < 2; ++n) { const f32x4 gk = __builtin_elementwise_fma(acc[ai][0][m][n], dsk, q.bg[n]), up = __builtin_elementwise_fma(acc[ai][1][m][n], dsu, q.bu[n]);
; #pragma unroll
;                         for (int j = 0; j < 4; ++j) { const float gm = __builtin_fmaxf(gk[j], 7.0f * KP), li = __builtin_amdgcn_fmed3f(up[j], -7.0f, 7.0f);
;                             const float sg = __builtin_amdgcn_rcpf(1.0f + __builtin_amdgcn_exp2f(gm));
;                             h[n * 4 + j] = (gm * sg) * (li * (FP8_SH / KP) + (FP8_SH / KP)); } }
;                     lo[mm] = pk4_fp8(h[0], h[1], h[2], h[3]); hi[mm] = pk4_fp8(h[4], h[5], h[6], h[7]); }
;                 const v2u r0 = __builtin_amdgcn_permlane16_swap(lo[0], lo[1], false, false), r1 = __builtin_amdgcn_permlane16_swap(hi[0], hi[1], false, false);
;                 unsigned char* rowp = hb + (size_t)(row0 + ai * 128 + (2 * mp + (fq & 1)) * 16) * FF + f0w + 16 * (fq >> 1);
;                 *(v4u*)rowp = (v4u){r0.x, r1.x, r0.y, r1.y}; }
;     }
	v_med3_f32 v22, v26, s94, v202
	v_mul_f32_e32 v21, v21, v189
	v_add_f32_e32 v11, 1.0, v11
	v_rcp_f32_e32 v189, v11
	v_exp_f32_e32 v11, v25
	v_mul_f32_e32 v31, v20, v21
	v_mul_f32_e32 v21, v23, v189
	v_add_f32_e32 v11, 1.0, v11
	v_rcp_f32_e32 v189, v11
	v_med3_f32 v24, v27, s94, v202
	v_mul_f32_e32 v11, v22, v21
	v_mul_f32_e32 v21, v25, v189
	v_pk_fma_f32 v[28:29], v[70:71], v[2:3], v[34:35]
	v_mul_f32_e32 v32, v24, v21
	v_pk_fma_f32 v[20:21], v[66:67], v[6:7], v[14:15]
	v_med3_f32 v22, v28, s94, v202
	v_max_f32_e32 v23, 0xc1898193, v20
	v_exp_f32_e32 v20, v23
	v_max_f32_e32 v21, 0xc1898193, v21
	v_pk_fma_f32 v[24:25], v[68:69], v[8:9], v[12:13]
	v_pk_fma_f32 v[26:27], v[72:73], v[4:5], v[36:37]
	v_add_f32_e32 v20, 1.0, v20
	v_rcp_f32_e32 v189, v20
	v_exp_f32_e32 v20, v21
	v_max_f32_e32 v25, 0xc1898193, v25
	v_pk_fma_f32 v[18:19], v[58:59], v[6:7], v[18:19]
	v_mul_f32_e32 v23, v23, v189
	v_add_f32_e32 v20, 1.0, v20
	v_mul_f32_e32 v28, v22, v23
	v_max_f32_e32 v23, 0xc1898193, v24
	v_exp_f32_e32 v22, v23
	v_rcp_f32_e32 v189, v20
	v_med3_f32 v20, v29, s94, v202
	v_exp_f32_e32 v24, v25
	v_add_f32_e32 v22, 1.0, v22
	v_mul_f32_e32 v21, v21, v189
	v_rcp_f32_e32 v189, v22
	v_med3_f32 v22, v26, s94, v202
	v_mul_f32_e32 v29, v20, v21
	v_mul_f32_e32 v21, v23, v189
	v_mov_b32_e32 v20, v22
	v_add_f32_e32 v22, 1.0, v24
	v_rcp_f32_e32 v189, v22
	v_mul_f32_e32 v26, v20, v21
	v_mov_b32_e32 v20, v187
	v_med3_f32 v24, v27, s94, v202
	v_cvt_pk_fp8_f32 v20, v30, v31
	v_mul_f32_e32 v23, v25, v189
	v_mov_b32_e32 v21, v187
	v_mul_f32_e32 v22, v24, v23
	v_max_f32_e32 v23, 0xc1898193, v18
	v_cvt_pk_fp8_f32 v20, v11, v32 op_sel:[0,0,1]
	v_exp_f32_e32 v11, v23
	v_cvt_pk_fp8_f32 v21, v28, v29
	v_max_f32_e32 v19, 0xc1898193, v19
	v_pk_fma_f32 v[16:17], v[60:61], v[8:9], v[16:17]
	v_add_f32_e32 v11, 1.0, v11
	v_rcp_f32_e32 v189, v11
	v_cvt_pk_fp8_f32 v21, v26, v22 op_sel:[0,0,1]
	v_pk_fma_f32 v[26:27], v[62:63], v[2:3], v[38:39]
	v_exp_f32_e32 v11, v19
	v_med3_f32 v22, v26, s94, v202
	v_mul_f32_e32 v23, v23, v189
	v_max_f32_e32 v17, 0xc1898193, v17
	v_mul_f32_e32 v26, v22, v23
	v_add_f32_e32 v11, 1.0, v11
	v_max_f32_e32 v23, 0xc1898193, v16
	v_rcp_f32_e32 v189, v11
	v_exp_f32_e32 v11, v23
	v_med3_f32 v18, v27, s94, v202
	v_pk_fma_f32 v[6:7], v[50:51], v[6:7], v[14:15]
	v_mul_f32_e32 v19, v19, v189
	v_add_f32_e32 v11, 1.0, v11
	v_rcp_f32_e32 v189, v11
	v_exp_f32_e32 v11, v17
	v_pk_fma_f32 v[24:25], v[64:65], v[4:5], v[40:41]
	v_max_f32_e32 v15, 0xc1898193, v6
	v_med3_f32 v22, v24, s94, v202
	v_add_f32_e32 v11, 1.0, v11
	v_exp_f32_e32 v6, v15
	v_mul_f32_e32 v27, v18, v19
	v_mul_f32_e32 v19, v23, v189
	v_mov_b32_e32 v18, v22
	v_rcp_f32_e32 v189, v11
	v_med3_f32 v16, v25, s94, v202
	v_add_f32_e32 v6, 1.0, v6
	v_pk_fma_f32 v[2:3], v[54:55], v[2:3], v[34:35]
	v_mul_f32_e32 v17, v17, v189
	v_rcp_f32_e32 v189, v6
	v_max_f32_e32 v7, 0xc1898193, v7
	v_med3_f32 v14, v2, s94, v202
	v_exp_f32_e32 v2, v7
	v_pk_fma_f32 v[8:9], v[52:53], v[8:9], v[12:13]
	v_mul_f32_e32 v13, v15, v189
	v_pk_fma_f32 v[4:5], v[56:57], v[4:5], v[36:37]
	v_mul_f32_e32 v14, v14, v13
	v_add_f32_e32 v2, 1.0, v2
	v_max_f32_e32 v13, 0xc1898193, v8
	v_rcp_f32_e32 v189, v2
	v_exp_f32_e32 v8, v13
	v_med3_f32 v6, v3, s94, v202
	v_med3_f32 v12, v4, s94, v202
	v_mul_f32_e32 v3, v7, v189
	v_mov_b32_e32 v2, v6
	v_add_f32_e32 v6, 1.0, v8
	v_max_f32_e32 v7, 0xc1898193, v9
	v_rcp_f32_e32 v189, v6
	v_exp_f32_e32 v6, v7
	v_mul_f32_e32 v8, v2, v3
	v_mul_f32_e32 v3, v13, v189
	v_add_f32_e32 v4, 1.0, v6
	v_rcp_f32_e32 v189, v4
	v_mov_b32_e32 v23, v187
	v_med3_f32 v6, v5, s94, v202
	v_mov_b32_e32 v22, v187
	v_cvt_pk_fp8_f32 v23, v14, v8
	v_mul_f32_e32 v4, v12, v3
	v_mul_f32_e32 v3, v7, v189
	v_cvt_pk_fp8_f32 v22, v26, v27
	v_mul_f32_e32 v2, v6, v3
	v_mul_f32_e32 v11, v18, v19
	v_mul_f32_e32 v16, v16, v17
	v_cvt_pk_fp8_f32 v23, v4, v2 op_sel:[0,0,1]
	v_add_u32_e32 v2, 0xa0, v10
	v_cvt_pk_fp8_f32 v22, v11, v16 op_sel:[0,0,1]
	v_ashrrev_i32_e32 v3, 31, v2
	v_lshlrev_b64 v[2:3], 11, v[2:3]
	v_lshl_add_u64 v[2:3], s[12:13], 0, v[2:3]
	v_lshl_add_u64 v[2:3], v[2:3], 0, s[26:27]
	v_permlane16_swap_b32_e32 v20, v22
	v_permlane16_swap_b32_e32 v21, v23
	v_lshl_add_u64 v[2:3], v[2:3], 0, v[186:187]
	global_store_dwordx4 v[2:3], v[20:23], off
	s_cbranch_vccnz .LBB0_726
	v_mov_b32_e32 v2, v0
	s_ashr_i32 s21, s20, 31
	v_readlane_b32 s72, v255, 29
	v_lshrrev_b32_e32 v2, 1, v2
	s_lshl_b64 s[2:3], s[20:21], 13
	v_readlane_b32 s76, v255, 33
	v_and_b32_e32 v2, 0x78, v2
	v_readlane_b32 s77, v255, 34
	s_add_u32 s26, s76, s2
	v_lshl_or_b32 v2, s44, 7, v2
	v_readlane_b32 s80, v255, 37
	s_addc_u32 s27, s77, s3
	v_ashrrev_i32_e32 v3, 31, v2
	v_readlane_b32 s81, v255, 38
	s_add_u32 s2, s80, s2
	v_lshlrev_b64 v[2:3], 2, v[2:3]
	s_addc_u32 s3, s81, s3
	v_lshl_add_u64 v[4:5], s[26:27], 0, v[2:3]
	v_lshl_add_u64 v[2:3], s[2:3], 0, v[2:3]
	global_load_dwordx4 v[74:77], v[4:5], off offset:16
	global_load_dwordx4 v[78:81], v[4:5], off
	global_load_dwordx4 v[34:37], v[2:3], off offset:16
	global_load_dwordx4 v[38:41], v[2:3], off
	v_readlane_b32 s2, v255, 53
	v_readlane_b32 s3, v255, 54
	s_andn2_b64 vcc, exec, s[2:3]
	v_readlane_b32 s73, v255, 30
	v_readlane_b32 s74, v255, 31
	v_readlane_b32 s75, v255, 32
	v_readlane_b32 s78, v255, 35
	v_readlane_b32 s79, v255, 36
	v_readlane_b32 s82, v255, 39
	v_readlane_b32 s83, v255, 40
	v_readlane_b32 s84, v255, 41
	v_readlane_b32 s85, v255, 42
	v_readlane_b32 s86, v255, 43
	v_readlane_b32 s87, v255, 44
	s_cbranch_vccnz .LBB0_725
	s_barrier
	s_branch .LBB0_725
